# P12: g_final quads loaded once before the row loop (no per-row reload ladder); plus P7/P2 epilogue hoists and moe_tables batching
# speedup vs baseline: 1.0080x; 1.0080x over previous
; DI void unpack8(const u32x4 r, f32x4& lo, f32x4& hi) { lo = (f32x4){bf_lo(r.x), bf_hi(r.x), bf_lo(r.y), bf_hi(r.y)}; hi = (f32x4){bf_lo(r.z), bf_hi(r.z), bf_lo(r.w), bf_hi(r.w)}; }
; DI void p11_final(const Params& P, int G, int bid) {
;     ...
;     for (int row = bid * 8 + wid; row < T; row += G * 8) {
;         const float* gt = modf + (size_t)(row / SEQ) * NMOD + 5 * D;
;         f32x4 v[8]; float ss = 0.f;
; #pragma unroll
;         for (int j = 0; j < 4; ++j) { const int c = 512 * j + 8 * lane; f32x4 m0 = {0.f, 0.f, 0.f, 0.f}, m1 = m0;
; #pragma unroll
;             for (int k = 0; k < 4; ++k) { const u32x2 y = *(const u32x2*)(YS + ((size_t)row * 4 + k) * D + c);
;                 const f32x2 a = __builtin_amdgcn_cvt_pk_f32_fp8((int)y.x, false), b = __builtin_amdgcn_cvt_pk_f32_fp8((int)y.x, true), cc = __builtin_amdgcn_cvt_pk_f32_fp8((int)y.y, false), d = __builtin_amdgcn_cvt_pk_f32_fp8((int)y.y, true);
;                 m0[0] += a[0]; m0[1] += a[1]; m0[2] += b[0]; m0[3] += b[1]; m1[0] += cc[0]; m1[1] += cc[1]; m1[2] += d[0]; m1[3] += d[1]; }
;             f32x4 x0, x1v; unpack8(*(const u32x4*)(X1 + (size_t)row * D + c), x0, x1v);
;             v[2 * j] = x0 + *(const f32x4*)(gt + c) * m0; v[2 * j + 1] = x1v + *(const f32x4*)(gt + c + 4) * m1;
.LBB0_1412:
	v_readlane_b32 s0, v254, 16
	v_readlane_b32 s1, v254, 17
	s_cmp_lt_i32 s0, 13
	s_cselect_b64 s[0:1], -1, 0
	s_and_b64 s[0:1], s[0:1], s[4:5]
	s_andn2_b64 vcc, exec, s[0:1]
	s_cbranch_vccnz .LBB0_1416
	s_getreg_b32 s0, hwreg(HW_REG_HW_ID, 0, 6)
	s_and_b32 s0, s0, 63
	s_lshl_b32 s0, s0, 2
	s_add_i32 s0, s0, 0
	s_add_i32 s0, s0, 0x24400
	v_mov_b32_e32 v0, s0
	ds_read_b32 v1, v0
	v_mbcnt_lo_u32_b32 v0, -1, 0
	v_mbcnt_hi_u32_b32 v0, -1, v0
	v_readlane_b32 s2, v254, 0
	s_lshl_b32 s1, s2, 3
	v_readlane_b32 s3, v254, 1
	s_waitcnt lgkmcnt(0)
	v_readfirstlane_b32 s0, v1
	s_nop 1
	v_lshl_add_u32 v1, s0, 6, v0
	s_nop 0
	v_readfirstlane_b32 s0, v1
	s_ashr_i32 s0, s0, 6
	s_add_i32 s10, s0, s1
	s_cmpk_gt_i32 s10, 0x7fff
	s_cbranch_scc1 .LBB0_1416
	v_lshlrev_b32_e32 v1, 3, v0
	v_readlane_b32 s2, v254, 18
	v_readlane_b32 s12, v254, 6
	v_and_b32_e32 v2, 0x1f8, v1
	v_readlane_b32 s3, v254, 19
	v_mov_b32_e32 v3, 0
	v_readlane_b32 s18, v254, 12
	v_readlane_b32 s19, v254, 13
	s_lshl_b32 s2, s2, 3
	v_or_b32_e32 v6, 0x400, v2
	v_lshlrev_b32_e32 v10, 2, v2
	v_mov_b32_e32 v11, v3
	s_mov_b64 s[6:7], s[18:19]
	s_ashr_i32 s3, s0, 31
	s_ashr_i32 s4, s1, 31
	v_or_b32_e32 v8, 0x600, v2
	v_readlane_b32 s13, v254, 7
	v_readlane_b32 s14, v254, 8
	v_readlane_b32 s15, v254, 9
	v_lshl_add_u64 v[12:13], s[6:7], 0, v[10:11]
	v_lshlrev_b32_e32 v10, 2, v6
	s_add_u32 s0, s0, s1
	v_lshl_add_u64 v[14:15], s[6:7], 0, v[10:11]
	v_lshlrev_b32_e32 v10, 2, v8
	s_addc_u32 s1, s3, s4
	v_readlane_b32 s12, v254, 2
	s_ashr_i32 s3, s2, 31
	v_lshl_add_u64 v[16:17], s[6:7], 0, v[10:11]
	s_lshl_b64 s[4:5], s[0:1], 13
	v_and_b32_e32 v5, 63, v0
	v_readlane_b32 s14, v254, 4
	s_lshl_b64 s[6:7], s[2:3], 13
	s_lshl_b64 s[0:1], s[0:1], 12
	v_lshlrev_b32_e32 v0, 5, v5
	v_mov_b32_e32 v1, v3
	v_readlane_b32 s13, v254, 3
	v_readlane_b32 s15, v254, 5
	s_add_u32 s0, s14, s0
	v_lshl_add_u64 v[18:19], s[12:13], 0, v[0:1]
	v_lshlrev_b32_e32 v0, 4, v5
	s_addc_u32 s1, s15, s1
	v_or_b32_e32 v4, 0x200, v2
	v_lshl_add_u64 v[0:1], s[0:1], 0, v[0:1]
	s_mov_b64 s[0:1], 0x74e00800
	v_lshl_add_u64 v[20:21], v[0:1], 0, s[0:1]
	s_lshl_b64 s[8:9], s[2:3], 12
	v_lshl_add_u64 v[22:23], s[14:15], 0, v[2:3]
	s_mov_b32 s3, 0x85a00000
	s_mov_b32 s11, 0x85a01000
	v_lshlrev_b32_e32 v26, 2, v2
	v_lshlrev_b32_e32 v27, 2, v4
	v_lshlrev_b32_e32 v28, 2, v6
	v_lshlrev_b32_e32 v29, 2, v8
	v_mov_b32_e32 v30, 0x358637bd
	v_mov_b32_e32 v31, 0x3a000000
	s_mov_b32 s12, 0xf800000
	v_mov_b32_e32 v32, 0x260
	s_movk_i32 s13, 0x1000
	v_readlane_b32 s16, v254, 10
	v_readlane_b32 s17, v254, 11
	global_load_dwordx4 v[220:223], v[12:13], off
	global_load_dwordx4 v[224:227], v[12:13], off offset:16
	global_load_dwordx4 v[228:231], v[12:13], off offset:2048
	global_load_dwordx4 v[232:235], v[12:13], off offset:2064
	global_load_dwordx4 v[236:239], v[14:15], off
	global_load_dwordx4 v[240:243], v[14:15], off offset:16
	global_load_dwordx4 v[244:247], v[16:17], off
	global_load_dwordx4 v[248:251], v[16:17], off offset:16
.LBB0_1415:
	v_lshl_add_u64 v[42:43], v[22:23], 0, s[4:5]
	v_add_co_u32_e32 v44, vcc, s3, v42
	s_ashr_i32 s0, s10, 31
	s_nop 0
	v_addc_co_u32_e32 v45, vcc, 0, v43, vcc
	v_add_co_u32_e32 v42, vcc, s11, v42
	s_lshr_b32 s0, s0, 18
	s_nop 0
	v_addc_co_u32_e32 v43, vcc, 0, v43, vcc
	global_load_dwordx4 v[0:3], v[20:21], off offset:-2048
	global_load_dwordx4 v[4:7], v[20:21], off offset:-1024
	global_load_dwordx4 v[34:37], v[20:21], off
	global_load_dwordx4 v[38:41], v[20:21], off offset:1024
	global_load_dwordx2 v[74:75], v[42:43], off offset:-4096
	global_load_dwordx2 v[76:77], v[44:45], off offset:2048
	global_load_dwordx2 v[78:79], v[42:43], off
	global_load_dwordx2 v[80:81], v[42:43], off offset:2048
	global_load_dwordx2 v[82:83], v[44:45], off offset:512
	global_load_dwordx2 v[84:85], v[44:45], off offset:2560
	s_add_i32 s0, s10, s0
	s_ashr_i32 s0, s0, 14
	s_mulk_i32 s0, 0x3000
	s_ashr_i32 s1, s0, 31
	global_load_dwordx2 v[86:87], v[42:43], off offset:512
	global_load_dwordx2 v[88:89], v[42:43], off offset:1024
	global_load_dwordx2 v[90:91], v[44:45], off offset:1024
	global_load_dwordx2 v[92:93], v[44:45], off offset:1536
	global_load_dwordx2 v[94:95], v[44:45], off offset:3072
	global_load_dwordx2 v[96:97], v[44:45], off offset:3584
	global_load_dwordx2 v[98:99], v[42:43], off offset:2560
	global_load_dwordx2 v[100:101], v[42:43], off offset:3072
	global_load_dwordx2 v[102:103], v[42:43], off offset:1536
	global_load_dwordx2 v[104:105], v[42:43], off offset:3584
	s_lshl_b64 s[0:1], s[0:1], 2
	s_add_u32 s0, s14, s0
	s_addc_u32 s1, s15, s1
	s_add_u32 s0, s0, 0x1ca000
	s_addc_u32 s1, s1, 0
	global_load_dwordx4 v[42:45], v26, s[0:1] offset:16
	global_load_dwordx4 v[46:49], v26, s[0:1]
	global_load_dwordx4 v[50:53], v27, s[0:1] offset:16
	global_load_dwordx4 v[54:57], v27, s[0:1]
	global_load_dwordx4 v[58:61], v28, s[0:1] offset:16
	global_load_dwordx4 v[62:65], v28, s[0:1]
	global_load_dwordx4 v[66:69], v29, s[0:1] offset:16
	global_load_dwordx4 v[70:73], v29, s[0:1]
	v_mov_b32_e32 v33, 0
	v_mov_b32_e32 v218, 0
	v_lshl_add_u64 v[24:25], v[18:19], 0, s[4:5]
	s_add_i32 s10, s10, s2
	v_lshl_add_u64 v[18:19], v[18:19], 0, s[6:7]
	v_lshl_add_u64 v[20:21], v[20:21], 0, s[8:9]
	v_lshl_add_u64 v[22:23], v[22:23], 0, s[6:7]
	s_cmp_lt_i32 s10, 0x8000
	s_waitcnt vmcnt(27)
	v_lshlrev_b32_e32 v106, 16, v0
	s_waitcnt vmcnt(23)
	v_cvt_pk_f32_fp8_e32 v[122:123], v74
	v_cvt_pk_f32_fp8_sdwa v[124:125], v74 src0_sel:WORD_1
	v_cvt_pk_f32_fp8_e32 v[126:127], v75
	v_cvt_pk_f32_fp8_sdwa v[74:75], v75 src0_sel:WORD_1
	s_waitcnt vmcnt(19)
; DI void unpack8(const u32x4 r, f32x4& lo, f32x4& hi) { lo = (f32x4){bf_lo(r.x), bf_hi(r.x), bf_lo(r.y), bf_hi(r.y)}; hi = (f32x4){bf_lo(r.z), bf_hi(r.z), bf_lo(r.w), bf_hi(r.w)}; }
; DI void p11_final(const Params& P, int G, int bid) {
;     ...
;             for (int k = 0; k < 4; ++k) { const u32x2 y = *(const u32x2*)(YS + ((size_t)row * 4 + k) * D + c);
;                 const f32x2 a = __builtin_amdgcn_cvt_pk_f32_fp8((int)y.x, false), b = __builtin_amdgcn_cvt_pk_f32_fp8((int)y.x, true), cc = __builtin_amdgcn_cvt_pk_f32_fp8((int)y.y, false), d = __builtin_amdgcn_cvt_pk_f32_fp8((int)y.y, true);
;                 m0[0] += a[0]; m0[1] += a[1]; m0[2] += b[0]; m0[3] += b[1]; m1[0] += cc[0]; m1[1] += cc[1]; m1[2] += d[0]; m1[3] += d[1]; }
;             f32x4 x0, x1v; unpack8(*(const u32x4*)(X1 + (size_t)row * D + c), x0, x1v);
	v_cvt_pk_f32_fp8_e32 v[146:147], v82
	v_cvt_pk_f32_fp8_sdwa v[148:149], v82 src0_sel:WORD_1
	v_cvt_pk_f32_fp8_e32 v[128:129], v76
	v_cvt_pk_f32_fp8_sdwa v[130:131], v76 src0_sel:WORD_1
	v_cvt_pk_f32_fp8_e32 v[132:133], v77
	v_cvt_pk_f32_fp8_sdwa v[76:77], v77 src0_sel:WORD_1
	v_cvt_pk_f32_fp8_e32 v[150:151], v83
	v_cvt_pk_f32_fp8_sdwa v[82:83], v83 src0_sel:WORD_1
	s_waitcnt vmcnt(18)
	v_cvt_pk_f32_fp8_e32 v[152:153], v84
	v_cvt_pk_f32_fp8_sdwa v[154:155], v84 src0_sel:WORD_1
	s_waitcnt vmcnt(15)
	v_cvt_pk_f32_fp8_e32 v[170:171], v90
	v_cvt_pk_f32_fp8_sdwa v[172:173], v90 src0_sel:WORD_1
	s_waitcnt vmcnt(14)
	v_cvt_pk_f32_fp8_e32 v[194:195], v92
	v_cvt_pk_f32_fp8_sdwa v[196:197], v92 src0_sel:WORD_1
	v_cvt_pk_f32_fp8_e32 v[198:199], v93
	v_cvt_pk_f32_fp8_sdwa v[92:93], v93 src0_sel:WORD_1
	v_cvt_pk_f32_fp8_e32 v[134:135], v78
	v_cvt_pk_f32_fp8_sdwa v[136:137], v78 src0_sel:WORD_1
	v_cvt_pk_f32_fp8_e32 v[138:139], v79
	v_cvt_pk_f32_fp8_sdwa v[78:79], v79 src0_sel:WORD_1
	v_cvt_pk_f32_fp8_e32 v[156:157], v85
	v_cvt_pk_f32_fp8_sdwa v[84:85], v85 src0_sel:WORD_1
	v_cvt_pk_f32_fp8_e32 v[158:159], v86
	v_cvt_pk_f32_fp8_sdwa v[160:161], v86 src0_sel:WORD_1
	v_cvt_pk_f32_fp8_e32 v[174:175], v91
	v_cvt_pk_f32_fp8_sdwa v[90:91], v91 src0_sel:WORD_1
	s_waitcnt vmcnt(13)
	v_cvt_pk_f32_fp8_e32 v[176:177], v94
	v_cvt_pk_f32_fp8_sdwa v[178:179], v94 src0_sel:WORD_1
	s_waitcnt vmcnt(12)
	v_cvt_pk_f32_fp8_e32 v[200:201], v96
	v_cvt_pk_f32_fp8_sdwa v[202:203], v96 src0_sel:WORD_1
	v_cvt_pk_f32_fp8_e32 v[204:205], v97
	v_cvt_pk_f32_fp8_sdwa v[96:97], v97 src0_sel:WORD_1
	v_cvt_pk_f32_fp8_e32 v[140:141], v80
	v_cvt_pk_f32_fp8_sdwa v[142:143], v80 src0_sel:WORD_1
	v_cvt_pk_f32_fp8_e32 v[144:145], v81
	v_cvt_pk_f32_fp8_sdwa v[80:81], v81 src0_sel:WORD_1
	v_cvt_pk_f32_fp8_e32 v[162:163], v87
	v_cvt_pk_f32_fp8_sdwa v[86:87], v87 src0_sel:WORD_1
	s_waitcnt vmcnt(11)
	v_cvt_pk_f32_fp8_e32 v[164:165], v98
	v_cvt_pk_f32_fp8_sdwa v[166:167], v98 src0_sel:WORD_1
	v_cvt_pk_f32_fp8_e32 v[180:181], v95
	v_cvt_pk_f32_fp8_sdwa v[94:95], v95 src0_sel:WORD_1
	v_cvt_pk_f32_fp8_e32 v[182:183], v88
	v_cvt_pk_f32_fp8_sdwa v[184:185], v88 src0_sel:WORD_1
	v_cvt_pk_f32_fp8_e32 v[168:169], v99
	v_cvt_pk_f32_fp8_sdwa v[98:99], v99 src0_sel:WORD_1
	v_cvt_pk_f32_fp8_e32 v[186:187], v89
	v_cvt_pk_f32_fp8_sdwa v[88:89], v89 src0_sel:WORD_1
	s_waitcnt vmcnt(10)
	v_cvt_pk_f32_fp8_e32 v[188:189], v100
	v_cvt_pk_f32_fp8_sdwa v[190:191], v100 src0_sel:WORD_1
	s_waitcnt vmcnt(9)
	v_cvt_pk_f32_fp8_e32 v[206:207], v102
	v_cvt_pk_f32_fp8_sdwa v[208:209], v102 src0_sel:WORD_1
	v_cvt_pk_f32_fp8_e32 v[210:211], v103
	v_cvt_pk_f32_fp8_sdwa v[102:103], v103 src0_sel:WORD_1
	v_pk_add_f32 v[124:125], v[124:125], 0 op_sel_hi:[1,0]
	v_pk_add_f32 v[122:123], v[122:123], 0 op_sel_hi:[1,0]
	v_pk_add_f32 v[74:75], v[74:75], 0 op_sel_hi:[1,0]
	v_pk_add_f32 v[148:149], v[148:149], 0 op_sel_hi:[1,0]
	v_pk_add_f32 v[146:147], v[146:147], 0 op_sel_hi:[1,0]
	v_cvt_pk_f32_fp8_e32 v[192:193], v101
	v_cvt_pk_f32_fp8_sdwa v[100:101], v101 src0_sel:WORD_1
	s_waitcnt vmcnt(8)
	v_cvt_pk_f32_fp8_e32 v[212:213], v104
	v_cvt_pk_f32_fp8_sdwa v[214:215], v104 src0_sel:WORD_1
	v_cvt_pk_f32_fp8_e32 v[216:217], v105
	v_pk_add_f32 v[126:127], v[126:127], 0 op_sel_hi:[1,0]
	v_pk_add_f32 v[82:83], v[82:83], 0 op_sel_hi:[1,0]
	v_pk_add_f32 v[150:151], v[150:151], 0 op_sel_hi:[1,0]
	v_pk_add_f32 v[172:173], v[172:173], 0 op_sel_hi:[1,0]
	v_pk_add_f32 v[170:171], v[170:171], 0 op_sel_hi:[1,0]
	v_pk_add_f32 v[92:93], v[92:93], 0 op_sel_hi:[1,0]
	v_pk_add_f32 v[122:123], v[122:123], v[128:129]
	v_pk_add_f32 v[124:125], v[124:125], v[130:131]
	v_pk_add_f32 v[74:75], v[74:75], v[76:77]
	v_pk_add_f32 v[76:77], v[146:147], v[152:153]
	v_pk_add_f32 v[128:129], v[148:149], v[154:155]
	v_cvt_pk_f32_fp8_sdwa v[104:105], v105 src0_sel:WORD_1
	v_pk_add_f32 v[90:91], v[90:91], 0 op_sel_hi:[1,0]
	v_pk_add_f32 v[174:175], v[174:175], 0 op_sel_hi:[1,0]
	v_pk_add_f32 v[196:197], v[196:197], 0 op_sel_hi:[1,0]
	v_pk_add_f32 v[194:195], v[194:195], 0 op_sel_hi:[1,0]
	v_pk_add_f32 v[198:199], v[198:199], 0 op_sel_hi:[1,0]
	v_pk_add_f32 v[126:127], v[126:127], v[132:133]
	v_pk_add_f32 v[130:131], v[150:151], v[156:157]
	v_pk_add_f32 v[82:83], v[82:83], v[84:85]
	v_pk_add_f32 v[84:85], v[170:171], v[176:177]
	v_pk_add_f32 v[132:133], v[172:173], v[178:179]
	v_pk_add_f32 v[92:93], v[92:93], v[96:97]
	v_pk_add_f32 v[96:97], v[124:125], v[136:137]
	v_pk_add_f32 v[122:123], v[122:123], v[134:135]
	v_pk_add_f32 v[74:75], v[74:75], v[78:79]
	v_pk_add_f32 v[124:125], v[128:129], v[160:161]
	v_pk_add_f32 v[76:77], v[76:77], v[158:159]
	v_and_b32_e32 v107, 0xffff0000, v0
	v_lshlrev_b32_e32 v0, 16, v1
	v_and_b32_e32 v1, 0xffff0000, v1
	v_lshlrev_b32_e32 v110, 16, v4
	v_and_b32_e32 v111, 0xffff0000, v4
	v_lshlrev_b32_e32 v4, 16, v5
	v_and_b32_e32 v5, 0xffff0000, v5
	v_pk_add_f32 v[146:147], v[174:175], v[180:181]
	v_pk_add_f32 v[90:91], v[90:91], v[94:95]
	v_pk_add_f32 v[94:95], v[194:195], v[200:201]
	v_pk_add_f32 v[148:149], v[196:197], v[202:203]
	v_pk_add_f32 v[150:151], v[198:199], v[204:205]
	v_pk_add_f32 v[78:79], v[126:127], v[138:139]
	v_pk_add_f32 v[82:83], v[82:83], v[86:87]
	v_pk_add_f32 v[86:87], v[130:131], v[162:163]
	v_pk_add_f32 v[126:127], v[132:133], v[184:185]
	v_pk_add_f32 v[84:85], v[84:85], v[182:183]
	v_pk_add_f32 v[122:123], v[122:123], v[140:141]
	v_pk_add_f32 v[96:97], v[96:97], v[142:143]
	v_pk_add_f32 v[74:75], v[74:75], v[80:81]
	v_pk_add_f32 v[76:77], v[76:77], v[164:165]
	v_pk_add_f32 v[80:81], v[124:125], v[166:167]
	v_lshlrev_b32_e32 v108, 16, v2
	v_and_b32_e32 v109, 0xffff0000, v2
	v_lshlrev_b32_e32 v2, 16, v3
	v_and_b32_e32 v3, 0xffff0000, v3
	v_lshlrev_b32_e32 v112, 16, v6
	v_and_b32_e32 v113, 0xffff0000, v6
	v_lshlrev_b32_e32 v6, 16, v7
	v_and_b32_e32 v7, 0xffff0000, v7
	v_lshlrev_b32_e32 v114, 16, v34
	v_and_b32_e32 v115, 0xffff0000, v34
	v_lshlrev_b32_e32 v34, 16, v35
	v_and_b32_e32 v35, 0xffff0000, v35
	v_pk_add_f32 v[88:89], v[90:91], v[88:89]
	v_pk_add_f32 v[90:91], v[146:147], v[186:187]
	v_pk_add_f32 v[128:129], v[148:149], v[208:209]
	v_pk_add_f32 v[94:95], v[94:95], v[206:207]
	v_pk_add_f32 v[92:93], v[92:93], v[102:103]
	v_pk_add_f32 v[102:103], v[150:151], v[210:211]
	v_pk_add_f32 v[78:79], v[78:79], v[144:145]
	v_pk_add_f32 v[86:87], v[86:87], v[168:169]
	v_pk_add_f32 v[82:83], v[82:83], v[98:99]
	v_pk_add_f32 v[84:85], v[84:85], v[188:189]
	v_pk_add_f32 v[98:99], v[126:127], v[190:191]
	s_waitcnt vmcnt(6)
; DI void p11_final(const Params& P, int G, int bid) {
;     ...
;             v[2 * j] = x0 + *(const f32x4*)(gt + c) * m0; v[2 * j + 1] = x1v + *(const f32x4*)(gt + c + 4) * m1;
;             ss += (v[2 * j][0] * v[2 * j][0] + v[2 * j][1] * v[2 * j][1]) + (v[2 * j][2] * v[2 * j][2] + v[2 * j][3] * v[2 * j][3]) + (v[2 * j + 1][0] * v[2 * j + 1][0] + v[2 * j + 1][1] * v[2 * j + 1][1]) + (v[2 * j + 1][2] * v[2 * j + 1][2] + v[2 * j + 1][3] * v[2 * j + 1][3]); }
;         const float rs = 1.0f / sqrtf(wave_sum(ss) * (1.0f / D) + EPS);
; #pragma unroll
;         for (int j = 0; j < 4; ++j) { const int c = 512 * j + 8 * lane; *(f32x4*)(P.out + (size_t)row * D + c) = v[2 * j] * rs * *(const f32x4*)(gfin + c); *(f32x4*)(P.out + (size_t)row * D + c + 4) = v[2 * j + 1] * rs * *(const f32x4*)(gfin + c + 4); }
	v_pk_fma_f32 v[0:1], v[48:49], v[96:97], v[0:1]
	v_pk_fma_f32 v[46:47], v[46:47], v[122:123], v[106:107]
	s_waitcnt vmcnt(4)
	v_pk_fma_f32 v[4:5], v[56:57], v[80:81], v[4:5]
	v_pk_fma_f32 v[48:49], v[54:55], v[76:77], v[110:111]
	v_lshlrev_b32_e32 v116, 16, v36
	v_and_b32_e32 v117, 0xffff0000, v36
	v_lshlrev_b32_e32 v36, 16, v37
	v_and_b32_e32 v37, 0xffff0000, v37
	v_lshlrev_b32_e32 v118, 16, v38
	v_and_b32_e32 v119, 0xffff0000, v38
	v_lshlrev_b32_e32 v38, 16, v39
	v_and_b32_e32 v39, 0xffff0000, v39
	v_lshlrev_b32_e32 v120, 16, v40
	v_and_b32_e32 v121, 0xffff0000, v40
	v_pk_add_f32 v[90:91], v[90:91], v[192:193]
	v_pk_add_f32 v[88:89], v[88:89], v[100:101]
	v_pk_add_f32 v[94:95], v[94:95], v[212:213]
	v_pk_add_f32 v[100:101], v[128:129], v[214:215]
	v_pk_add_f32 v[102:103], v[102:103], v[216:217]
	v_pk_fma_f32 v[44:45], v[44:45], v[74:75], v[2:3]
	v_pk_fma_f32 v[42:43], v[42:43], v[78:79], v[108:109]
	v_pk_fma_f32 v[6:7], v[52:53], v[82:83], v[6:7]
	v_pk_fma_f32 v[50:51], v[50:51], v[86:87], v[112:113]
	s_waitcnt vmcnt(2)
	v_pk_fma_f32 v[34:35], v[64:65], v[98:99], v[34:35]
	v_pk_fma_f32 v[52:53], v[62:63], v[84:85], v[114:115]
	v_mul_f32_e32 v2, v47, v47
	v_mul_f32_e32 v3, v1, v1
	v_mul_f32_e32 v62, v49, v49
	v_mul_f32_e32 v63, v5, v5
	v_lshlrev_b32_e32 v40, 16, v41
	v_and_b32_e32 v41, 0xffff0000, v41
	v_pk_add_f32 v[92:93], v[92:93], v[104:105]
	v_pk_fma_f32 v[36:37], v[60:61], v[88:89], v[36:37]
	v_pk_fma_f32 v[54:55], v[58:59], v[90:91], v[116:117]
	s_waitcnt vmcnt(0)
	v_pk_fma_f32 v[38:39], v[72:73], v[100:101], v[38:39]
	v_pk_fma_f32 v[56:57], v[70:71], v[94:95], v[118:119]
	v_pk_fma_f32 v[58:59], v[66:67], v[102:103], v[120:121]
	v_mul_f32_e32 v60, v43, v43
	v_mul_f32_e32 v64, v51, v51
	v_mul_f32_e32 v66, v53, v53
	v_mul_f32_e32 v67, v35, v35
	v_fmac_f32_e32 v2, v46, v46
	v_fmac_f32_e32 v3, v0, v0
	v_fmac_f32_e32 v62, v48, v48
	v_fmac_f32_e32 v63, v4, v4
	v_pk_fma_f32 v[40:41], v[68:69], v[92:93], v[40:41]
	v_mul_f32_e32 v61, v45, v45
	v_mul_f32_e32 v65, v7, v7
	v_mul_f32_e32 v68, v55, v55
	v_mul_f32_e32 v70, v57, v57
	v_mul_f32_e32 v71, v39, v39
	v_fmac_f32_e32 v60, v42, v42
	v_fmac_f32_e32 v64, v50, v50
	v_fmac_f32_e32 v66, v52, v52
	v_fmac_f32_e32 v67, v34, v34
	v_add_f32_e32 v2, v2, v3
	v_add_f32_e32 v3, v62, v63
	v_mul_f32_e32 v69, v37, v37
	v_mul_f32_e32 v72, v59, v59
	v_fmac_f32_e32 v61, v44, v44
	v_fmac_f32_e32 v65, v6, v6
	v_fmac_f32_e32 v68, v54, v54
	v_fmac_f32_e32 v70, v56, v56
	v_fmac_f32_e32 v71, v38, v38
	v_add_f32_e32 v62, v66, v67
	v_add_f32_e32 v2, v60, v2
	v_add_f32_e32 v3, v64, v3
	v_mul_f32_e32 v73, v41, v41
	v_fmac_f32_e32 v69, v36, v36
	v_fmac_f32_e32 v72, v58, v58
	v_add_f32_e32 v63, v70, v71
	v_add_f32_e32 v60, v68, v62
	v_add_f32_e32 v2, v61, v2
	v_add_f32_e32 v3, v65, v3
	v_fmac_f32_e32 v73, v40, v40
	v_add_f32_e32 v62, v72, v63
	v_add_f32_e32 v60, v69, v60
	v_add_f32_e32 v2, v2, v3
	v_add_f32_e32 v61, v73, v62
	v_add_f32_e32 v2, v2, v60
	v_add_f32_e32 v2, v2, v61
	s_nop 1
	v_add_f32_dpp v2, v2, v2 quad_perm:[1,0,3,2] row_mask:0xf bank_mask:0xf bound_ctrl:1
	s_nop 1
	v_add_f32_dpp v2, v2, v2 quad_perm:[2,3,0,1] row_mask:0xf bank_mask:0xf bound_ctrl:1
	s_nop 1
	v_add_f32_dpp v2, v2, v2 row_ror:4 row_mask:0xf bank_mask:0xf bound_ctrl:1
	s_nop 1
	v_add_f32_dpp v2, v2, v2 row_ror:8 row_mask:0xf bank_mask:0xf bound_ctrl:1
	s_nop 1
	v_mov_b32_dpp v33, v2 row_bcast:15 row_mask:0xa bank_mask:0xf
	v_add_f32_e32 v2, v2, v33
	s_nop 1
	v_mov_b32_dpp v218, v2 row_bcast:31 row_mask:0xc bank_mask:0xf
	v_add_f32_e32 v2, v2, v218
	s_nop 0
	v_readlane_b32 s0, v2, 63
	s_nop 1
	v_fma_f32 v2, s0, v31, v30
	v_mul_f32_e32 v3, 0x4f800000, v2
	v_cmp_gt_f32_e32 vcc, s12, v2
	s_nop 1
	v_cndmask_b32_e32 v2, v2, v3, vcc
	v_sqrt_f32_e32 v3, v2
	s_nop 0
	v_add_u32_e32 v33, -1, v3
	v_add_u32_e32 v60, 1, v3
	v_fma_f32 v61, -v33, v3, v2
	v_fma_f32 v62, -v60, v3, v2
	v_cmp_ge_f32_e64 s[0:1], 0, v61
	s_nop 1
	v_cndmask_b32_e64 v3, v3, v33, s[0:1]
	v_cmp_lt_f32_e64 s[0:1], 0, v62
	s_nop 1
	v_cndmask_b32_e64 v3, v3, v60, s[0:1]
	v_mul_f32_e32 v33, 0x37800000, v3
	v_cndmask_b32_e32 v3, v3, v33, vcc
	v_cmp_class_f32_e32 vcc, v2, v32
	s_nop 1
	v_cndmask_b32_e32 v2, v3, v2, vcc
	v_div_scale_f32 v3, s[0:1], v2, v2, 1.0
	v_rcp_f32_e32 v60, v3
	v_div_scale_f32 v33, vcc, 1.0, v2, 1.0
	v_fma_f32 v61, -v3, v60, 1.0
	v_fmac_f32_e32 v60, v61, v60
	v_mul_f32_e32 v61, v33, v60
	v_fma_f32 v62, -v3, v61, v33
	v_fmac_f32_e32 v61, v62, v60
	v_fma_f32 v3, -v3, v61, v33
	v_div_fmas_f32 v3, v3, v60, v61
	v_div_fixup_f32 v60, v3, v2, 1.0
	v_pk_mul_f32 v[46:47], v[46:47], v[60:61] op_sel_hi:[1,0]
	v_pk_mul_f32 v[0:1], v[0:1], v[60:61] op_sel_hi:[1,0]
	v_pk_mul_f32 v[4:5], v[4:5], v[60:61] op_sel_hi:[1,0]
	v_pk_mul_f32 v[2:3], v[222:223], v[0:1]
	v_pk_mul_f32 v[0:1], v[220:221], v[46:47]
	global_store_dwordx4 v[24:25], v[0:3], off
	v_pk_mul_f32 v[8:9], v[44:45], v[60:61] op_sel_hi:[1,0]
	v_pk_mul_f32 v[10:11], v[42:43], v[60:61] op_sel_hi:[1,0]
	v_pk_mul_f32 v[2:3], v[226:227], v[8:9]
	v_pk_mul_f32 v[0:1], v[224:225], v[10:11]
	global_store_dwordx4 v[24:25], v[0:3], off offset:16
	v_pk_mul_f32 v[8:9], v[48:49], v[60:61] op_sel_hi:[1,0]
	s_nop 0
	v_pk_mul_f32 v[2:3], v[230:231], v[4:5]
	v_pk_mul_f32 v[0:1], v[228:229], v[8:9]
	global_store_dwordx4 v[24:25], v[0:3], off offset:2048
	v_pk_mul_f32 v[4:5], v[6:7], v[60:61] op_sel_hi:[1,0]
	v_pk_mul_f32 v[6:7], v[50:51], v[60:61] op_sel_hi:[1,0]
	v_pk_mul_f32 v[8:9], v[52:53], v[60:61] op_sel_hi:[1,0]
	v_pk_mul_f32 v[0:1], v[6:7], v[232:233]
	v_pk_mul_f32 v[2:3], v[4:5], v[234:235]
	global_store_dwordx4 v[24:25], v[0:3], off offset:2064
	v_add_co_u32_e32 v4, vcc, s13, v24
	v_pk_mul_f32 v[6:7], v[34:35], v[60:61] op_sel_hi:[1,0]
	s_nop 0
	v_addc_co_u32_e32 v5, vcc, 0, v25, vcc
	v_pk_mul_f32 v[0:1], v[8:9], v[236:237]
	v_pk_mul_f32 v[2:3], v[6:7], v[238:239]
	global_store_dwordx4 v[4:5], v[0:3], off
	v_pk_mul_f32 v[6:7], v[36:37], v[60:61] op_sel_hi:[1,0]
	v_pk_mul_f32 v[8:9], v[54:55], v[60:61] op_sel_hi:[1,0]
	v_pk_mul_f32 v[2:3], v[6:7], v[242:243]
	v_pk_mul_f32 v[0:1], v[8:9], v[240:241]
	global_store_dwordx4 v[4:5], v[0:3], off offset:16
	v_pk_mul_f32 v[6:7], v[38:39], v[60:61] op_sel_hi:[1,0]
	v_pk_mul_f32 v[8:9], v[56:57], v[60:61] op_sel_hi:[1,0]
	v_pk_mul_f32 v[2:3], v[6:7], v[246:247]
	v_pk_mul_f32 v[0:1], v[8:9], v[244:245]
	global_store_dwordx4 v[4:5], v[0:3], off offset:2048
	v_pk_mul_f32 v[6:7], v[40:41], v[60:61] op_sel_hi:[1,0]
	v_pk_mul_f32 v[8:9], v[58:59], v[60:61] op_sel_hi:[1,0]
	v_pk_mul_f32 v[2:3], v[6:7], v[250:251]
	v_pk_mul_f32 v[0:1], v[8:9], v[248:249]
	global_store_dwordx4 v[4:5], v[0:3], off offset:2064
	s_cbranch_scc1 .LBB0_1415
